# scan state waves: hand-scheduled block with all LDS operands fetched ahead (registers of the helper staging set), same MFMA/VALU math and order; plus the helper triangular-inverse rewrite
# baseline (speedup 1.0000x reference)
.LBB0_1114:
	v_writelane_b32 v255, s0, 11
	s_and_b32 s5, s0, 1
	v_readlane_b32 s0, v254, 35
	v_readlane_b32 s1, v254, 36
	s_andn2_b64 vcc, exec, s[0:1]
	s_mov_b64 s[76:77], -1
	v_cndmask_b32_e64 v18, 0, 1, s[0:1]
	v_cmp_ne_u32_e64 s[8:9], 1, v18
	s_mul_i32 s0, s5, 0x1e00
	v_add_u32_e32 v34, v115, v155
	v_writelane_b32 v255, s8, 17
	v_add_u32_e32 v35, v115, v117
	v_add_u32_e32 v193, 0, v113
	v_writelane_b32 v255, s9, 18
	v_add_u32_e32 v36, v115, v156
	v_add_u32_e32 v192, s0, v166
	v_writelane_b32 v255, s5, 13
	v_lshl_add_u32 v191, s5, 13, v165
	s_cbranch_vccnz .LBB0_1116
	v_readlane_b32 s0, v255, 13
	v_add_u32_e32 v246, v115, v155
	v_add_u32_e32 v248, v115, v117
	s_nop 0
	s_mul_i32 s1, s0, 0x1e00
	s_lshl_b32 s0, s0, 13
	v_mov_b32_e32 v250, v116
	v_mov_b32_e32 v251, v113
	v_add_u32_e32 v249, 0x5c00, v248
	v_add_u32_e32 v248, 0x4800, v248
	v_add_u32_e32 v252, s1, v166
	v_add_u32_e32 v253, s0, v165
	v_add_u32_e32 v247, 0x1200, v246
	ds_read2_b64 v[18:21], v246 offset1:4
	ds_read2_b64 v[22:25], v246 offset0:8 offset1:12
	ds_read_b64 v[66:67], v250 offset:28672
	ds_read2_b64 v[68:71], v252 offset1:80
	v_cvt_pk_bf16_f32 v198, v2, v3
	v_cvt_pk_bf16_f32 v199, v4, v5
	v_cvt_pk_bf16_f32 v202, v10, v11
	v_cvt_pk_bf16_f32 v203, v12, v13
	v_cvt_pk_bf16_f32 v200, v6, v7
	v_cvt_pk_bf16_f32 v201, v8, v9
	v_cvt_pk_bf16_f32 v204, v14, v15
	v_cvt_pk_bf16_f32 v205, v16, v17
	ds_read2_b64 v[26:29], v247 offset1:4
	ds_read2_b64 v[30:33], v247 offset0:8 offset1:12
	ds_read2_b64 v[72:75], v252 offset0:160 offset1:240
	s_waitcnt lgkmcnt(6)
	v_mfma_f32_16x16x16_bf16 v[206:209], v[18:19], v[198:199], 0
	s_waitcnt lgkmcnt(5)
	v_mfma_f32_16x16x16_bf16 v[210:213], v[22:23], v[202:203], 0
	ds_read2_b64 v[34:37], v248 offset1:80
	ds_read2_b64 v[38:41], v248 offset0:160 offset1:240
	v_mfma_f32_16x16x16_bf16 v[206:209], v[20:21], v[200:201], v[206:209]
	v_mfma_f32_16x16x16_bf16 v[210:213], v[24:25], v[204:205], v[210:213]
	ds_read2_b64 v[42:45], v249 offset1:80
	ds_read2_b64 v[46:49], v249 offset0:160 offset1:240
	s_waitcnt lgkmcnt(8)
	s_waitcnt lgkmcnt(7)
	v_mfma_f32_16x16x16_bf16 v[210:213], v[68:69], v[66:67], v[210:213]
	s_waitcnt lgkmcnt(6)
	v_mfma_f32_16x16x16_bf16 v[214:217], v[26:27], v[198:199], 0
	s_waitcnt lgkmcnt(5)
	v_mfma_f32_16x16x16_bf16 v[218:221], v[30:31], v[202:203], 0
	v_mfma_f32_16x16x16_bf16 v[214:217], v[28:29], v[200:201], v[214:217]
	v_mfma_f32_16x16x16_bf16 v[218:221], v[32:33], v[204:205], v[218:221]
	ds_read_b128 v[50:53], v251 offset:33792
	ds_read_b128 v[54:57], v251 offset:33856
	ds_read_b128 v[58:61], v251 offset:33920
	ds_read_b128 v[62:65], v251 offset:33984
	v_add_u32_e32 v246, 0x900, v246
	ds_read2_b64 v[76:79], v246 offset1:4
	ds_read2_b64 v[80:83], v246 offset0:8 offset1:12
	v_pk_add_f32 v[206:207], v[206:207], v[210:211]
	v_pk_add_f32 v[208:209], v[208:209], v[212:213]
	v_cvt_pk_bf16_f32 v242, v206, v207
	v_cvt_pk_bf16_f32 v243, v208, v209
	ds_read_b64 v[84:85], v250 offset:31232
	v_add_u32_e32 v252, 0xf00, v252
	ds_read2_b64 v[86:89], v252 offset1:80
	s_waitcnt lgkmcnt(12)
	v_mfma_f32_16x16x16_bf16 v[238:241], v[74:75], v[242:243], 0
	v_mfma_f32_16x16x16_bf16 v[214:217], v[70:71], v[66:67], v[214:217]
	s_waitcnt lgkmcnt(11)
	v_mfma_f32_16x16x16_bf16 v[2:5], v[34:35], v[66:67], v[2:5]
	v_mfma_f32_16x16x16_bf16 v[6:9], v[36:37], v[66:67], v[6:9]
	s_waitcnt lgkmcnt(10)
	v_mfma_f32_16x16x16_bf16 v[10:13], v[38:39], v[66:67], v[10:13]
	v_mfma_f32_16x16x16_bf16 v[14:17], v[40:41], v[66:67], v[14:17]
	ds_read2_b64 v[90:93], v252 offset0:160 offset1:240
	v_add_u32_e32 v247, 0x900, v247
	ds_read2_b64 v[26:29], v247 offset1:4
	ds_read2_b64 v[30:33], v247 offset0:8 offset1:12
	v_cvt_pk_bf16_f32 v244, -v238, -v239
	v_cvt_pk_bf16_f32 v245, -v240, -v241
	v_add_u32_e32 v248, 0xa00, v248
	ds_read2_b64 v[34:37], v248 offset1:80
	s_waitcnt lgkmcnt(13)
	ds_read2_b64 v[38:41], v248 offset0:160 offset1:240
	v_mfma_f32_16x16x16_bf16 v[2:5], v[42:43], v[244:245], v[2:5]
	v_mfma_f32_16x16x16_bf16 v[6:9], v[44:45], v[244:245], v[6:9]
	s_waitcnt lgkmcnt(13)
	v_mfma_f32_16x16x16_bf16 v[10:13], v[46:47], v[244:245], v[10:13]
	v_mfma_f32_16x16x16_bf16 v[14:17], v[48:49], v[244:245], v[14:17]
	v_mfma_f32_16x16x16_bf16 v[218:221], v[72:73], v[244:245], v[218:221]
	v_add_u32_e32 v249, 0xa00, v249
	ds_read2_b64 v[42:45], v249 offset1:80
	s_waitcnt lgkmcnt(13)
	ds_read2_b64 v[46:49], v249 offset0:160 offset1:240
	v_pk_mul_f32 v[2:3], v[50:51], v[2:3]
	v_pk_mul_f32 v[4:5], v[52:53], v[4:5]
	s_waitcnt lgkmcnt(13)
	v_pk_mul_f32 v[6:7], v[54:55], v[6:7]
	v_pk_mul_f32 v[8:9], v[56:57], v[8:9]
	s_waitcnt lgkmcnt(12)
	v_pk_mul_f32 v[10:11], v[58:59], v[10:11]
	v_pk_mul_f32 v[12:13], v[60:61], v[12:13]
	s_waitcnt lgkmcnt(11)
	v_pk_mul_f32 v[14:15], v[62:63], v[14:15]
	v_pk_mul_f32 v[16:17], v[64:65], v[16:17]
	v_pk_add_f32 v[214:215], v[214:215], v[218:219]
	v_pk_add_f32 v[216:217], v[216:217], v[220:221]
	ds_write2st64_b32 v253, v214, v215 offset0:0 offset1:1
	ds_write2st64_b32 v253, v216, v217 offset0:2 offset1:3
	ds_read_b128 v[50:53], v251 offset:34048
	s_waitcnt lgkmcnt(13)
	ds_read_b128 v[54:57], v251 offset:34112
	s_waitcnt lgkmcnt(13)
	ds_read_b128 v[58:61], v251 offset:34176
	s_waitcnt lgkmcnt(13)
	ds_read_b128 v[62:65], v251 offset:34240
	v_cvt_pk_bf16_f32 v198, v2, v3
	v_cvt_pk_bf16_f32 v199, v4, v5
	v_cvt_pk_bf16_f32 v202, v10, v11
	v_cvt_pk_bf16_f32 v203, v12, v13
	v_cvt_pk_bf16_f32 v200, v6, v7
	v_cvt_pk_bf16_f32 v201, v8, v9
	v_cvt_pk_bf16_f32 v204, v14, v15
	v_cvt_pk_bf16_f32 v205, v16, v17
	v_mfma_f32_16x16x16_bf16 v[206:209], v[76:77], v[198:199], 0
	v_mfma_f32_16x16x16_bf16 v[210:213], v[80:81], v[202:203], 0
	v_mfma_f32_16x16x16_bf16 v[206:209], v[78:79], v[200:201], v[206:209]
	v_mfma_f32_16x16x16_bf16 v[210:213], v[82:83], v[204:205], v[210:213]
	s_waitcnt lgkmcnt(13)
	v_mfma_f32_16x16x16_bf16 v[210:213], v[86:87], v[84:85], v[210:213]
	s_waitcnt lgkmcnt(11)
	v_mfma_f32_16x16x16_bf16 v[214:217], v[26:27], v[198:199], 0
	s_waitcnt lgkmcnt(10)
	v_mfma_f32_16x16x16_bf16 v[218:221], v[30:31], v[202:203], 0
	v_mfma_f32_16x16x16_bf16 v[214:217], v[28:29], v[200:201], v[214:217]
	v_mfma_f32_16x16x16_bf16 v[218:221], v[32:33], v[204:205], v[218:221]
	s_nop 1
	v_pk_add_f32 v[206:207], v[206:207], v[210:211]
	v_pk_add_f32 v[208:209], v[208:209], v[212:213]
	v_cvt_pk_bf16_f32 v242, v206, v207
	v_cvt_pk_bf16_f32 v243, v208, v209
	s_nop 1
	v_mfma_f32_16x16x16_bf16 v[238:241], v[92:93], v[242:243], 0
	v_mfma_f32_16x16x16_bf16 v[214:217], v[88:89], v[84:85], v[214:217]
	s_waitcnt lgkmcnt(9)
	v_mfma_f32_16x16x16_bf16 v[2:5], v[34:35], v[84:85], v[2:5]
	v_mfma_f32_16x16x16_bf16 v[6:9], v[36:37], v[84:85], v[6:9]
	s_waitcnt lgkmcnt(8)
	v_mfma_f32_16x16x16_bf16 v[10:13], v[38:39], v[84:85], v[10:13]
	v_mfma_f32_16x16x16_bf16 v[14:17], v[40:41], v[84:85], v[14:17]
	s_nop 0
	v_cvt_pk_bf16_f32 v244, -v238, -v239
	v_cvt_pk_bf16_f32 v245, -v240, -v241
	s_waitcnt lgkmcnt(7)
	s_nop 0
	v_mfma_f32_16x16x16_bf16 v[2:5], v[42:43], v[244:245], v[2:5]
	v_mfma_f32_16x16x16_bf16 v[6:9], v[44:45], v[244:245], v[6:9]
	s_waitcnt lgkmcnt(6)
	v_mfma_f32_16x16x16_bf16 v[10:13], v[46:47], v[244:245], v[10:13]
	v_mfma_f32_16x16x16_bf16 v[14:17], v[48:49], v[244:245], v[14:17]
	v_mfma_f32_16x16x16_bf16 v[218:221], v[90:91], v[244:245], v[218:221]
	s_waitcnt lgkmcnt(3)
	s_nop 1
	v_pk_mul_f32 v[2:3], v[50:51], v[2:3]
	v_pk_mul_f32 v[4:5], v[52:53], v[4:5]
	s_waitcnt lgkmcnt(2)
	v_pk_mul_f32 v[6:7], v[54:55], v[6:7]
	v_pk_mul_f32 v[8:9], v[56:57], v[8:9]
	s_waitcnt lgkmcnt(1)
	v_pk_mul_f32 v[10:11], v[58:59], v[10:11]
	v_pk_mul_f32 v[12:13], v[60:61], v[12:13]
	s_waitcnt lgkmcnt(0)
	v_pk_mul_f32 v[14:15], v[62:63], v[14:15]
	v_pk_mul_f32 v[16:17], v[64:65], v[16:17]
	v_pk_add_f32 v[214:215], v[214:215], v[218:219]
	v_pk_add_f32 v[216:217], v[216:217], v[220:221]
	ds_write2st64_b32 v253, v214, v215 offset0:16 offset1:17
	ds_write2st64_b32 v253, v216, v217 offset0:18 offset1:19
	s_branch .Lscan_join1

.LBB0_1140:
.Lscan_join1:
	s_waitcnt lgkmcnt(0)
	s_barrier
	v_readlane_b32 s0, v255, 17
	v_readlane_b32 s1, v255, 18
	s_and_b64 vcc, exec, s[0:1]
	s_mov_b64 s[76:77], -1
	s_cbranch_vccnz .LBB0_1142
	v_readlane_b32 s0, v255, 13
	v_add_u32_e32 v246, v115, v155
	v_add_u32_e32 v248, v115, v117
	s_xor_b32 s0, s0, 1
	s_mul_i32 s1, s0, 0x1e00
	s_lshl_b32 s0, s0, 13
	v_add_u32_e32 v246, 0x8600, v246
	v_add_u32_e32 v250, 0x8600, v116
	v_add_u32_e32 v251, 0x8600, v113
	v_add_u32_e32 v249, 0xe200, v248
	v_add_u32_e32 v248, 0xce00, v248
	v_add_u32_e32 v252, s1, v166
	v_add_u32_e32 v253, s0, v165
	v_add_u32_e32 v247, 0x1200, v246
	ds_read2_b64 v[18:21], v246 offset1:4
	ds_read2_b64 v[22:25], v246 offset0:8 offset1:12
	ds_read_b64 v[66:67], v250 offset:28672
	ds_read2_b64 v[68:71], v252 offset1:80
	v_cvt_pk_bf16_f32 v198, v2, v3
	v_cvt_pk_bf16_f32 v199, v4, v5
	v_cvt_pk_bf16_f32 v202, v10, v11
	v_cvt_pk_bf16_f32 v203, v12, v13
	v_cvt_pk_bf16_f32 v200, v6, v7
	v_cvt_pk_bf16_f32 v201, v8, v9
	v_cvt_pk_bf16_f32 v204, v14, v15
	v_cvt_pk_bf16_f32 v205, v16, v17
	ds_read2_b64 v[26:29], v247 offset1:4
	ds_read2_b64 v[30:33], v247 offset0:8 offset1:12
	ds_read2_b64 v[72:75], v252 offset0:160 offset1:240
	s_waitcnt lgkmcnt(6)
	v_mfma_f32_16x16x16_bf16 v[206:209], v[18:19], v[198:199], 0
	s_waitcnt lgkmcnt(5)
	v_mfma_f32_16x16x16_bf16 v[210:213], v[22:23], v[202:203], 0
	ds_read2_b64 v[34:37], v248 offset1:80
	ds_read2_b64 v[38:41], v248 offset0:160 offset1:240
	v_mfma_f32_16x16x16_bf16 v[206:209], v[20:21], v[200:201], v[206:209]
	v_mfma_f32_16x16x16_bf16 v[210:213], v[24:25], v[204:205], v[210:213]
	ds_read2_b64 v[42:45], v249 offset1:80
	ds_read2_b64 v[46:49], v249 offset0:160 offset1:240
	s_waitcnt lgkmcnt(8)
	s_waitcnt lgkmcnt(7)
	v_mfma_f32_16x16x16_bf16 v[210:213], v[68:69], v[66:67], v[210:213]
	s_waitcnt lgkmcnt(6)
	v_mfma_f32_16x16x16_bf16 v[214:217], v[26:27], v[198:199], 0
	s_waitcnt lgkmcnt(5)
	v_mfma_f32_16x16x16_bf16 v[218:221], v[30:31], v[202:203], 0
	v_mfma_f32_16x16x16_bf16 v[214:217], v[28:29], v[200:201], v[214:217]
	v_mfma_f32_16x16x16_bf16 v[218:221], v[32:33], v[204:205], v[218:221]
	ds_read_b128 v[50:53], v251 offset:33792
	ds_read_b128 v[54:57], v251 offset:33856
	ds_read_b128 v[58:61], v251 offset:33920
	ds_read_b128 v[62:65], v251 offset:33984
	v_add_u32_e32 v246, 0x900, v246
	ds_read2_b64 v[76:79], v246 offset1:4
	ds_read2_b64 v[80:83], v246 offset0:8 offset1:12
	v_pk_add_f32 v[206:207], v[206:207], v[210:211]
	v_pk_add_f32 v[208:209], v[208:209], v[212:213]
	v_cvt_pk_bf16_f32 v242, v206, v207
	v_cvt_pk_bf16_f32 v243, v208, v209
	ds_read_b64 v[84:85], v250 offset:31232
	v_add_u32_e32 v252, 0xf00, v252
	ds_read2_b64 v[86:89], v252 offset1:80
	s_waitcnt lgkmcnt(12)
	v_mfma_f32_16x16x16_bf16 v[238:241], v[74:75], v[242:243], 0
	v_mfma_f32_16x16x16_bf16 v[214:217], v[70:71], v[66:67], v[214:217]
	s_waitcnt lgkmcnt(11)
	v_mfma_f32_16x16x16_bf16 v[2:5], v[34:35], v[66:67], v[2:5]
	v_mfma_f32_16x16x16_bf16 v[6:9], v[36:37], v[66:67], v[6:9]
	s_waitcnt lgkmcnt(10)
	v_mfma_f32_16x16x16_bf16 v[10:13], v[38:39], v[66:67], v[10:13]
	v_mfma_f32_16x16x16_bf16 v[14:17], v[40:41], v[66:67], v[14:17]
	ds_read2_b64 v[90:93], v252 offset0:160 offset1:240
	v_add_u32_e32 v247, 0x900, v247
	ds_read2_b64 v[26:29], v247 offset1:4
	ds_read2_b64 v[30:33], v247 offset0:8 offset1:12
	v_cvt_pk_bf16_f32 v244, -v238, -v239
	v_cvt_pk_bf16_f32 v245, -v240, -v241
	v_add_u32_e32 v248, 0xa00, v248
	ds_read2_b64 v[34:37], v248 offset1:80
	s_waitcnt lgkmcnt(13)
	ds_read2_b64 v[38:41], v248 offset0:160 offset1:240
	v_mfma_f32_16x16x16_bf16 v[2:5], v[42:43], v[244:245], v[2:5]
	v_mfma_f32_16x16x16_bf16 v[6:9], v[44:45], v[244:245], v[6:9]
	s_waitcnt lgkmcnt(13)
	v_mfma_f32_16x16x16_bf16 v[10:13], v[46:47], v[244:245], v[10:13]
	v_mfma_f32_16x16x16_bf16 v[14:17], v[48:49], v[244:245], v[14:17]
	v_mfma_f32_16x16x16_bf16 v[218:221], v[72:73], v[244:245], v[218:221]
	v_add_u32_e32 v249, 0xa00, v249
	ds_read2_b64 v[42:45], v249 offset1:80
	s_waitcnt lgkmcnt(13)
	ds_read2_b64 v[46:49], v249 offset0:160 offset1:240
	v_pk_mul_f32 v[2:3], v[50:51], v[2:3]
	v_pk_mul_f32 v[4:5], v[52:53], v[4:5]
	s_waitcnt lgkmcnt(13)
	v_pk_mul_f32 v[6:7], v[54:55], v[6:7]
	v_pk_mul_f32 v[8:9], v[56:57], v[8:9]
	s_waitcnt lgkmcnt(12)
	v_pk_mul_f32 v[10:11], v[58:59], v[10:11]
	v_pk_mul_f32 v[12:13], v[60:61], v[12:13]
	s_waitcnt lgkmcnt(11)
	v_pk_mul_f32 v[14:15], v[62:63], v[14:15]
	v_pk_mul_f32 v[16:17], v[64:65], v[16:17]
	v_pk_add_f32 v[214:215], v[214:215], v[218:219]
	v_pk_add_f32 v[216:217], v[216:217], v[220:221]
	ds_write2st64_b32 v253, v214, v215 offset0:0 offset1:1
	ds_write2st64_b32 v253, v216, v217 offset0:2 offset1:3
	ds_read_b128 v[50:53], v251 offset:34048
	s_waitcnt lgkmcnt(13)
	ds_read_b128 v[54:57], v251 offset:34112
	s_waitcnt lgkmcnt(13)
	ds_read_b128 v[58:61], v251 offset:34176
	s_waitcnt lgkmcnt(13)
	ds_read_b128 v[62:65], v251 offset:34240
	v_cvt_pk_bf16_f32 v198, v2, v3
	v_cvt_pk_bf16_f32 v199, v4, v5
	v_cvt_pk_bf16_f32 v202, v10, v11
	v_cvt_pk_bf16_f32 v203, v12, v13
	v_cvt_pk_bf16_f32 v200, v6, v7
	v_cvt_pk_bf16_f32 v201, v8, v9
	v_cvt_pk_bf16_f32 v204, v14, v15
	v_cvt_pk_bf16_f32 v205, v16, v17
	v_mfma_f32_16x16x16_bf16 v[206:209], v[76:77], v[198:199], 0
	v_mfma_f32_16x16x16_bf16 v[210:213], v[80:81], v[202:203], 0
	v_mfma_f32_16x16x16_bf16 v[206:209], v[78:79], v[200:201], v[206:209]
	v_mfma_f32_16x16x16_bf16 v[210:213], v[82:83], v[204:205], v[210:213]
	s_waitcnt lgkmcnt(13)
	v_mfma_f32_16x16x16_bf16 v[210:213], v[86:87], v[84:85], v[210:213]
	s_waitcnt lgkmcnt(11)
	v_mfma_f32_16x16x16_bf16 v[214:217], v[26:27], v[198:199], 0
	s_waitcnt lgkmcnt(10)
	v_mfma_f32_16x16x16_bf16 v[218:221], v[30:31], v[202:203], 0
	v_mfma_f32_16x16x16_bf16 v[214:217], v[28:29], v[200:201], v[214:217]
	v_mfma_f32_16x16x16_bf16 v[218:221], v[32:33], v[204:205], v[218:221]
	s_nop 1
	v_pk_add_f32 v[206:207], v[206:207], v[210:211]
	v_pk_add_f32 v[208:209], v[208:209], v[212:213]
	v_cvt_pk_bf16_f32 v242, v206, v207
	v_cvt_pk_bf16_f32 v243, v208, v209
	s_nop 1
	v_mfma_f32_16x16x16_bf16 v[238:241], v[92:93], v[242:243], 0
	v_mfma_f32_16x16x16_bf16 v[214:217], v[88:89], v[84:85], v[214:217]
	s_waitcnt lgkmcnt(9)
	v_mfma_f32_16x16x16_bf16 v[2:5], v[34:35], v[84:85], v[2:5]
	v_mfma_f32_16x16x16_bf16 v[6:9], v[36:37], v[84:85], v[6:9]
	s_waitcnt lgkmcnt(8)
	v_mfma_f32_16x16x16_bf16 v[10:13], v[38:39], v[84:85], v[10:13]
	v_mfma_f32_16x16x16_bf16 v[14:17], v[40:41], v[84:85], v[14:17]
	s_nop 0
	v_cvt_pk_bf16_f32 v244, -v238, -v239
	v_cvt_pk_bf16_f32 v245, -v240, -v241
	s_waitcnt lgkmcnt(7)
	s_nop 0
	v_mfma_f32_16x16x16_bf16 v[2:5], v[42:43], v[244:245], v[2:5]
	v_mfma_f32_16x16x16_bf16 v[6:9], v[44:45], v[244:245], v[6:9]
	s_waitcnt lgkmcnt(6)
	v_mfma_f32_16x16x16_bf16 v[10:13], v[46:47], v[244:245], v[10:13]
	v_mfma_f32_16x16x16_bf16 v[14:17], v[48:49], v[244:245], v[14:17]
	v_mfma_f32_16x16x16_bf16 v[218:221], v[90:91], v[244:245], v[218:221]
	s_waitcnt lgkmcnt(3)
	s_nop 1
	v_pk_mul_f32 v[2:3], v[50:51], v[2:3]
	v_pk_mul_f32 v[4:5], v[52:53], v[4:5]
	s_waitcnt lgkmcnt(2)
	v_pk_mul_f32 v[6:7], v[54:55], v[6:7]
	v_pk_mul_f32 v[8:9], v[56:57], v[8:9]
	s_waitcnt lgkmcnt(1)
	v_pk_mul_f32 v[10:11], v[58:59], v[10:11]
	v_pk_mul_f32 v[12:13], v[60:61], v[12:13]
	s_waitcnt lgkmcnt(0)
	v_pk_mul_f32 v[14:15], v[62:63], v[14:15]
	v_pk_mul_f32 v[16:17], v[64:65], v[16:17]
	v_pk_add_f32 v[214:215], v[214:215], v[218:219]
	v_pk_add_f32 v[216:217], v[216:217], v[220:221]
	ds_write2st64_b32 v253, v214, v215 offset0:16 offset1:17
	ds_write2st64_b32 v253, v216, v217 offset0:18 offset1:19
	s_branch .Lscan_join2

.LBB0_1160:
.Lscan_join2:
	s_waitcnt lgkmcnt(0)
	s_barrier
	v_readlane_b32 s0, v255, 17
	v_readlane_b32 s1, v255, 18
	s_and_b64 vcc, exec, s[0:1]
	s_mov_b64 s[30:31], -1
	s_cbranch_vccnz .LBB0_1162
	v_readlane_b32 s0, v255, 13
	v_add_u32_e32 v246, v115, v155
	v_add_u32_e32 v248, v115, v117
	s_nop 0
	s_mul_i32 s1, s0, 0x1e00
	s_lshl_b32 s0, s0, 13
	v_add_u32_e32 v246, 0x10c00, v246
	v_add_u32_e32 v250, 0x10c00, v116
	v_add_u32_e32 v251, 0x10c00, v113
	v_add_u32_e32 v249, 0x16800, v248
	v_add_u32_e32 v248, 0x15400, v248
	v_add_u32_e32 v252, s1, v166
	v_add_u32_e32 v253, s0, v165
	v_add_u32_e32 v247, 0x1200, v246
	ds_read2_b64 v[18:21], v246 offset1:4
	ds_read2_b64 v[22:25], v246 offset0:8 offset1:12
	ds_read_b64 v[66:67], v250 offset:28672
	ds_read2_b64 v[68:71], v252 offset1:80
	v_cvt_pk_bf16_f32 v198, v2, v3
	v_cvt_pk_bf16_f32 v199, v4, v5
	v_cvt_pk_bf16_f32 v202, v10, v11
	v_cvt_pk_bf16_f32 v203, v12, v13
	v_cvt_pk_bf16_f32 v200, v6, v7
	v_cvt_pk_bf16_f32 v201, v8, v9
	v_cvt_pk_bf16_f32 v204, v14, v15
	v_cvt_pk_bf16_f32 v205, v16, v17
	ds_read2_b64 v[26:29], v247 offset1:4
	ds_read2_b64 v[30:33], v247 offset0:8 offset1:12
	ds_read2_b64 v[72:75], v252 offset0:160 offset1:240
	s_waitcnt lgkmcnt(6)
	v_mfma_f32_16x16x16_bf16 v[206:209], v[18:19], v[198:199], 0
	s_waitcnt lgkmcnt(5)
	v_mfma_f32_16x16x16_bf16 v[210:213], v[22:23], v[202:203], 0
	ds_read2_b64 v[34:37], v248 offset1:80
	ds_read2_b64 v[38:41], v248 offset0:160 offset1:240
	v_mfma_f32_16x16x16_bf16 v[206:209], v[20:21], v[200:201], v[206:209]
	v_mfma_f32_16x16x16_bf16 v[210:213], v[24:25], v[204:205], v[210:213]
	ds_read2_b64 v[42:45], v249 offset1:80
	ds_read2_b64 v[46:49], v249 offset0:160 offset1:240
	s_waitcnt lgkmcnt(8)
	s_waitcnt lgkmcnt(7)
	v_mfma_f32_16x16x16_bf16 v[210:213], v[68:69], v[66:67], v[210:213]
	s_waitcnt lgkmcnt(6)
	v_mfma_f32_16x16x16_bf16 v[214:217], v[26:27], v[198:199], 0
	s_waitcnt lgkmcnt(5)
	v_mfma_f32_16x16x16_bf16 v[218:221], v[30:31], v[202:203], 0
	v_mfma_f32_16x16x16_bf16 v[214:217], v[28:29], v[200:201], v[214:217]
	v_mfma_f32_16x16x16_bf16 v[218:221], v[32:33], v[204:205], v[218:221]
	ds_read_b128 v[50:53], v251 offset:33792
	ds_read_b128 v[54:57], v251 offset:33856
	ds_read_b128 v[58:61], v251 offset:33920
	ds_read_b128 v[62:65], v251 offset:33984
	v_add_u32_e32 v246, 0x900, v246
	ds_read2_b64 v[76:79], v246 offset1:4
	ds_read2_b64 v[80:83], v246 offset0:8 offset1:12
	v_pk_add_f32 v[206:207], v[206:207], v[210:211]
	v_pk_add_f32 v[208:209], v[208:209], v[212:213]
	v_cvt_pk_bf16_f32 v242, v206, v207
	v_cvt_pk_bf16_f32 v243, v208, v209
	ds_read_b64 v[84:85], v250 offset:31232
	v_add_u32_e32 v252, 0xf00, v252
	ds_read2_b64 v[86:89], v252 offset1:80
	s_waitcnt lgkmcnt(12)
	v_mfma_f32_16x16x16_bf16 v[238:241], v[74:75], v[242:243], 0
	v_mfma_f32_16x16x16_bf16 v[214:217], v[70:71], v[66:67], v[214:217]
	s_waitcnt lgkmcnt(11)
	v_mfma_f32_16x16x16_bf16 v[2:5], v[34:35], v[66:67], v[2:5]
	v_mfma_f32_16x16x16_bf16 v[6:9], v[36:37], v[66:67], v[6:9]
	s_waitcnt lgkmcnt(10)
	v_mfma_f32_16x16x16_bf16 v[10:13], v[38:39], v[66:67], v[10:13]
	v_mfma_f32_16x16x16_bf16 v[14:17], v[40:41], v[66:67], v[14:17]
	ds_read2_b64 v[90:93], v252 offset0:160 offset1:240
	v_add_u32_e32 v247, 0x900, v247
	ds_read2_b64 v[26:29], v247 offset1:4
	ds_read2_b64 v[30:33], v247 offset0:8 offset1:12
	v_cvt_pk_bf16_f32 v244, -v238, -v239
	v_cvt_pk_bf16_f32 v245, -v240, -v241
	v_add_u32_e32 v248, 0xa00, v248
	ds_read2_b64 v[34:37], v248 offset1:80
	s_waitcnt lgkmcnt(13)
	ds_read2_b64 v[38:41], v248 offset0:160 offset1:240
	v_mfma_f32_16x16x16_bf16 v[2:5], v[42:43], v[244:245], v[2:5]
	v_mfma_f32_16x16x16_bf16 v[6:9], v[44:45], v[244:245], v[6:9]
	s_waitcnt lgkmcnt(13)
	v_mfma_f32_16x16x16_bf16 v[10:13], v[46:47], v[244:245], v[10:13]
	v_mfma_f32_16x16x16_bf16 v[14:17], v[48:49], v[244:245], v[14:17]
	v_mfma_f32_16x16x16_bf16 v[218:221], v[72:73], v[244:245], v[218:221]
	v_add_u32_e32 v249, 0xa00, v249
	ds_read2_b64 v[42:45], v249 offset1:80
	s_waitcnt lgkmcnt(13)
	ds_read2_b64 v[46:49], v249 offset0:160 offset1:240
	v_pk_mul_f32 v[2:3], v[50:51], v[2:3]
	v_pk_mul_f32 v[4:5], v[52:53], v[4:5]
	s_waitcnt lgkmcnt(13)
	v_pk_mul_f32 v[6:7], v[54:55], v[6:7]
	v_pk_mul_f32 v[8:9], v[56:57], v[8:9]
	s_waitcnt lgkmcnt(12)
	v_pk_mul_f32 v[10:11], v[58:59], v[10:11]
	v_pk_mul_f32 v[12:13], v[60:61], v[12:13]
	s_waitcnt lgkmcnt(11)
	v_pk_mul_f32 v[14:15], v[62:63], v[14:15]
	v_pk_mul_f32 v[16:17], v[64:65], v[16:17]
	v_pk_add_f32 v[214:215], v[214:215], v[218:219]
	v_pk_add_f32 v[216:217], v[216:217], v[220:221]
	ds_write2st64_b32 v253, v214, v215 offset0:0 offset1:1
	ds_write2st64_b32 v253, v216, v217 offset0:2 offset1:3
	ds_read_b128 v[50:53], v251 offset:34048
	s_waitcnt lgkmcnt(13)
	ds_read_b128 v[54:57], v251 offset:34112
	s_waitcnt lgkmcnt(13)
	ds_read_b128 v[58:61], v251 offset:34176
	s_waitcnt lgkmcnt(13)
	ds_read_b128 v[62:65], v251 offset:34240
	v_cvt_pk_bf16_f32 v198, v2, v3
	v_cvt_pk_bf16_f32 v199, v4, v5
	v_cvt_pk_bf16_f32 v202, v10, v11
	v_cvt_pk_bf16_f32 v203, v12, v13
	v_cvt_pk_bf16_f32 v200, v6, v7
	v_cvt_pk_bf16_f32 v201, v8, v9
	v_cvt_pk_bf16_f32 v204, v14, v15
	v_cvt_pk_bf16_f32 v205, v16, v17
	v_mfma_f32_16x16x16_bf16 v[206:209], v[76:77], v[198:199], 0
	v_mfma_f32_16x16x16_bf16 v[210:213], v[80:81], v[202:203], 0
	v_mfma_f32_16x16x16_bf16 v[206:209], v[78:79], v[200:201], v[206:209]
	v_mfma_f32_16x16x16_bf16 v[210:213], v[82:83], v[204:205], v[210:213]
	s_waitcnt lgkmcnt(13)
	v_mfma_f32_16x16x16_bf16 v[210:213], v[86:87], v[84:85], v[210:213]
	s_waitcnt lgkmcnt(11)
	v_mfma_f32_16x16x16_bf16 v[214:217], v[26:27], v[198:199], 0
	s_waitcnt lgkmcnt(10)
	v_mfma_f32_16x16x16_bf16 v[218:221], v[30:31], v[202:203], 0
	v_mfma_f32_16x16x16_bf16 v[214:217], v[28:29], v[200:201], v[214:217]
	v_mfma_f32_16x16x16_bf16 v[218:221], v[32:33], v[204:205], v[218:221]
	s_nop 1
	v_pk_add_f32 v[206:207], v[206:207], v[210:211]
	v_pk_add_f32 v[208:209], v[208:209], v[212:213]
	v_cvt_pk_bf16_f32 v242, v206, v207
	v_cvt_pk_bf16_f32 v243, v208, v209
	s_nop 1
	v_mfma_f32_16x16x16_bf16 v[238:241], v[92:93], v[242:243], 0
	v_mfma_f32_16x16x16_bf16 v[214:217], v[88:89], v[84:85], v[214:217]
	s_waitcnt lgkmcnt(9)
	v_mfma_f32_16x16x16_bf16 v[2:5], v[34:35], v[84:85], v[2:5]
	v_mfma_f32_16x16x16_bf16 v[6:9], v[36:37], v[84:85], v[6:9]
	s_waitcnt lgkmcnt(8)
	v_mfma_f32_16x16x16_bf16 v[10:13], v[38:39], v[84:85], v[10:13]
	v_mfma_f32_16x16x16_bf16 v[14:17], v[40:41], v[84:85], v[14:17]
	s_nop 0
	v_cvt_pk_bf16_f32 v244, -v238, -v239
	v_cvt_pk_bf16_f32 v245, -v240, -v241
	s_waitcnt lgkmcnt(7)
	s_nop 0
	v_mfma_f32_16x16x16_bf16 v[2:5], v[42:43], v[244:245], v[2:5]
	v_mfma_f32_16x16x16_bf16 v[6:9], v[44:45], v[244:245], v[6:9]
	s_waitcnt lgkmcnt(6)
	v_mfma_f32_16x16x16_bf16 v[10:13], v[46:47], v[244:245], v[10:13]
	v_mfma_f32_16x16x16_bf16 v[14:17], v[48:49], v[244:245], v[14:17]
	v_mfma_f32_16x16x16_bf16 v[218:221], v[90:91], v[244:245], v[218:221]
	s_waitcnt lgkmcnt(3)
	s_nop 1
	v_pk_mul_f32 v[2:3], v[50:51], v[2:3]
	v_pk_mul_f32 v[4:5], v[52:53], v[4:5]
	s_waitcnt lgkmcnt(2)
	v_pk_mul_f32 v[6:7], v[54:55], v[6:7]
	v_pk_mul_f32 v[8:9], v[56:57], v[8:9]
	s_waitcnt lgkmcnt(1)
	v_pk_mul_f32 v[10:11], v[58:59], v[10:11]
	v_pk_mul_f32 v[12:13], v[60:61], v[12:13]
	s_waitcnt lgkmcnt(0)
	v_pk_mul_f32 v[14:15], v[62:63], v[14:15]
	v_pk_mul_f32 v[16:17], v[64:65], v[16:17]
	v_pk_add_f32 v[214:215], v[214:215], v[218:219]
	v_pk_add_f32 v[216:217], v[216:217], v[220:221]
	ds_write2st64_b32 v253, v214, v215 offset0:16 offset1:17
	ds_write2st64_b32 v253, v216, v217 offset0:18 offset1:19
	v_mov_b64_e32 v[18:19], v[2:3]
	v_mov_b64_e32 v[20:21], v[4:5]
	v_mov_b64_e32 v[22:23], v[6:7]
	v_mov_b64_e32 v[24:25], v[8:9]
	v_mov_b64_e32 v[26:27], v[10:11]
	v_mov_b64_e32 v[28:29], v[12:13]
	v_mov_b64_e32 v[30:31], v[14:15]
	v_mov_b64_e32 v[32:33], v[16:17]
	s_branch .Lscan_join3

.LBB0_1186:
.Lscan_join3:
	s_waitcnt lgkmcnt(0)
	s_barrier
	v_readlane_b32 s5, v255, 11
	v_readlane_b32 s1, v255, 25
	s_add_i32 s0, s5, 3
	s_addk_i32 s4, 0x60
	s_addk_i32 s1, 0x1800
	v_writelane_b32 v255, s1, 25
	s_cmpk_gt_u32 s5, 0x44
	v_add_u32_e32 v190, 0xffffffa0, v190
	s_cbranch_scc1 .LBB0_1188
	v_mov_b32_e32 v2, v18
	v_mov_b32_e32 v3, v19
	v_mov_b32_e32 v4, v20
	v_mov_b32_e32 v5, v21
	v_mov_b32_e32 v6, v22
	v_mov_b32_e32 v7, v23
	v_mov_b32_e32 v8, v24
	v_mov_b32_e32 v9, v25
	v_mov_b32_e32 v10, v26
	v_mov_b32_e32 v11, v27
	v_mov_b32_e32 v12, v28
	v_mov_b32_e32 v13, v29
	v_mov_b32_e32 v14, v30
	v_mov_b32_e32 v15, v31
	v_mov_b32_e32 v16, v32
	v_mov_b32_e32 v17, v33
	s_branch .LBB0_1114
